# phase J layer 1 row tail: 16 loads (x1 row + gate row) issued up front into free VGPRs, per-step vmcnt(7), instead of 8 serialized load-wait-fma-store round trips
# speedup vs baseline: 1.0082x; 1.0011x over previous
.LBB0_4008:
	s_ashr_i32 s1, s0, 31
	s_lshl_b64 s[10:11], s[0:1], 13
	v_lshl_add_u64 v[58:59], v[46:47], 0, s[10:11]
	v_lshl_add_u64 v[60:61], v[48:49], 0, s[10:11]
	v_add_co_u32_e32 v174, vcc, s5, v58
	s_nop 1
	v_addc_co_u32_e32 v175, vcc, 0, v59, vcc
	v_add_co_u32_e32 v176, vcc, s5, v60
	s_nop 1
	v_addc_co_u32_e32 v177, vcc, 0, v61, vcc
	global_load_dwordx4 v[110:113], v[58:59], off
	global_load_dwordx4 v[114:117], v[58:59], off offset:1024
	global_load_dwordx4 v[118:121], v[58:59], off offset:2048
	global_load_dwordx4 v[122:125], v[58:59], off offset:3072
	global_load_dwordx4 v[126:129], v[174:175], off
	global_load_dwordx4 v[130:133], v[174:175], off offset:1024
	global_load_dwordx4 v[134:137], v[174:175], off offset:2048
	global_load_dwordx4 v[138:141], v[174:175], off offset:3072
	global_load_dwordx4 v[142:145], v[36:37], off
	global_load_dwordx4 v[146:149], v[36:37], off offset:1024
	global_load_dwordx4 v[150:153], v[36:37], off offset:2048
	global_load_dwordx4 v[154:157], v[36:37], off offset:3072
	global_load_dwordx4 v[158:161], v[38:39], off
	global_load_dwordx4 v[162:165], v[40:41], off
	global_load_dwordx4 v[166:169], v[42:43], off
	global_load_dwordx4 v[170:173], v[44:45], off
	s_add_i32 s0, s0, s4
	s_add_u32 s6, s6, s8
	s_addc_u32 s7, s7, s9
	s_cmpk_gt_i32 s0, 0x3fff
	s_waitcnt vmcnt(7)
	v_pk_fma_f32 v[2:3], v[2:3], v[142:143], v[110:111]
	v_pk_fma_f32 v[4:5], v[4:5], v[144:145], v[112:113]
	global_store_dwordx4 v[60:61], v[2:5], off
	s_waitcnt vmcnt(7)
	v_pk_fma_f32 v[6:7], v[6:7], v[146:147], v[114:115]
	v_pk_fma_f32 v[8:9], v[8:9], v[148:149], v[116:117]
	global_store_dwordx4 v[60:61], v[6:9], off offset:1024
	s_waitcnt vmcnt(7)
	v_pk_fma_f32 v[10:11], v[10:11], v[150:151], v[118:119]
	v_pk_fma_f32 v[12:13], v[12:13], v[152:153], v[120:121]
	global_store_dwordx4 v[60:61], v[10:13], off offset:2048
	s_waitcnt vmcnt(7)
	v_pk_fma_f32 v[14:15], v[14:15], v[154:155], v[122:123]
	v_pk_fma_f32 v[16:17], v[16:17], v[156:157], v[124:125]
	global_store_dwordx4 v[60:61], v[14:17], off offset:3072
	s_waitcnt vmcnt(7)
	v_pk_fma_f32 v[18:19], v[18:19], v[158:159], v[126:127]
	v_pk_fma_f32 v[20:21], v[20:21], v[160:161], v[128:129]
	global_store_dwordx4 v[176:177], v[18:21], off
	s_waitcnt vmcnt(7)
	v_pk_fma_f32 v[22:23], v[22:23], v[162:163], v[130:131]
	v_pk_fma_f32 v[24:25], v[24:25], v[164:165], v[132:133]
	global_store_dwordx4 v[176:177], v[22:25], off offset:1024
	s_waitcnt vmcnt(7)
	v_pk_fma_f32 v[26:27], v[26:27], v[166:167], v[134:135]
	v_pk_fma_f32 v[28:29], v[28:29], v[168:169], v[136:137]
	global_store_dwordx4 v[176:177], v[26:29], off offset:2048
	s_waitcnt vmcnt(7)
	v_pk_fma_f32 v[30:31], v[30:31], v[170:171], v[138:139]
	v_pk_fma_f32 v[32:33], v[32:33], v[172:173], v[140:141]
	global_store_dwordx4 v[176:177], v[30:33], off offset:3072
	s_cbranch_scc1 .LBB0_4013
